# combo7 + P8 epilogue: current-unit slot loads first, next-unit mask prefetch behind them, counted wait vmcnt(16), mask reduction moved to the epilogue end (prefetch miss latency overlaps the scatter)
# speedup vs baseline: 1.0163x; 1.0039x over previous
.LBB0_943:
	s_lshl_b32 s25, s34, 6
	s_add_i32 s36, s25, s36
	s_ashr_i32 s37, s36, 31
	s_lshl_b64 s[36:37], s[36:37], 16
	v_lshl_add_u64 v[0:1], v[170:171], 0, s[36:37]
	v_add_co_u32_e32 v2, vcc, 0x1000, v0
	s_nop 1
	v_addc_co_u32_e32 v3, vcc, 0, v1, vcc
	v_add_co_u32_e32 v4, vcc, 0x2000, v0
	s_nop 1
	v_addc_co_u32_e32 v5, vcc, 0, v1, vcc
	v_add_co_u32_e32 v6, vcc, 0x3000, v0
	s_nop 1
	v_addc_co_u32_e32 v7, vcc, 0, v1, vcc
	global_load_dwordx2 v[182:183], v[0:1], off
	global_load_dwordx2 v[30:31], v[2:3], off
	global_load_dwordx2 v[28:29], v[4:5], off
	global_load_dwordx2 v[26:27], v[6:7], off
	v_add_co_u32_e32 v2, vcc, 0x4000, v0
	s_nop 1
	v_addc_co_u32_e32 v3, vcc, 0, v1, vcc
	v_add_co_u32_e32 v4, vcc, 0x5000, v0
	s_nop 1
	v_addc_co_u32_e32 v5, vcc, 0, v1, vcc
	v_add_co_u32_e32 v6, vcc, 0x6000, v0
	s_nop 1
	v_addc_co_u32_e32 v7, vcc, 0, v1, vcc
	v_add_co_u32_e32 v8, vcc, 0x7000, v0
	s_nop 1
	v_addc_co_u32_e32 v9, vcc, 0, v1, vcc
	global_load_dwordx2 v[24:25], v[2:3], off
	global_load_dwordx2 v[22:23], v[4:5], off
	global_load_dwordx2 v[20:21], v[6:7], off
	global_load_dwordx2 v[18:19], v[8:9], off
	v_add_co_u32_e32 v2, vcc, 0x8000, v0
	s_nop 1
	v_addc_co_u32_e32 v3, vcc, 0, v1, vcc
	v_add_co_u32_e32 v4, vcc, 0x9000, v0
	s_nop 1
	v_addc_co_u32_e32 v5, vcc, 0, v1, vcc
	v_add_co_u32_e32 v6, vcc, 0xa000, v0
	s_nop 1
	v_addc_co_u32_e32 v7, vcc, 0, v1, vcc
	v_add_co_u32_e32 v8, vcc, 0xb000, v0
	s_nop 1
	v_addc_co_u32_e32 v9, vcc, 0, v1, vcc
	global_load_dwordx2 v[16:17], v[2:3], off
	global_load_dwordx2 v[14:15], v[4:5], off
	global_load_dwordx2 v[12:13], v[6:7], off
	global_load_dwordx2 v[10:11], v[8:9], off
	v_add_co_u32_e32 v2, vcc, 0xc000, v0
	s_nop 1
	v_addc_co_u32_e32 v3, vcc, 0, v1, vcc
	v_add_co_u32_e32 v4, vcc, 0xd000, v0
	s_nop 1
	v_addc_co_u32_e32 v5, vcc, 0, v1, vcc
	v_add_co_u32_e32 v180, vcc, 0xe000, v0
	s_nop 1
	v_addc_co_u32_e32 v181, vcc, 0, v1, vcc
	v_add_co_u32_e32 v0, vcc, 0xf000, v0
	s_nop 1
	v_addc_co_u32_e32 v1, vcc, 0, v1, vcc
	global_load_dwordx2 v[8:9], v[2:3], off
	global_load_dwordx2 v[6:7], v[4:5], off
	s_nop 0
	global_load_dwordx2 v[2:3], v[180:181], off
	s_nop 0
	global_load_dwordx2 v[0:1], v[0:1], off
	v_lshl_add_u32 v4, s34, 8, v188
	v_ashrrev_i32_e32 v5, 31, v4
	v_lshlrev_b64 v[180:181], 9, v[4:5]
	v_lshl_add_u64 v[180:181], s[10:11], 0, v[180:181]
	s_mov_b32 s75, -1
	s_cmp_lg_u64 s[4:5], 0
	s_cbranch_scc0 .Lp8n_skip
	s_lshl_b32 s76, s26, 6
	s_add_i32 s76, s76, s24
	s_ashr_i32 s77, s76, 31
	s_lshl_b64 s[76:77], s[76:77], 16
	v_lshl_add_u64 v[186:187], v[170:171], 0, s[76:77]
	s_mov_b64 s[76:77], 0x1000
	global_load_dwordx2 v[208:209], v[186:187], off
	v_lshl_add_u64 v[186:187], v[186:187], 0, s[76:77]
	global_load_dwordx2 v[210:211], v[186:187], off
	v_lshl_add_u64 v[186:187], v[186:187], 0, s[76:77]
	global_load_dwordx2 v[212:213], v[186:187], off
	v_lshl_add_u64 v[186:187], v[186:187], 0, s[76:77]
	global_load_dwordx2 v[214:215], v[186:187], off
	v_lshl_add_u64 v[186:187], v[186:187], 0, s[76:77]
	global_load_dwordx2 v[216:217], v[186:187], off
	v_lshl_add_u64 v[186:187], v[186:187], 0, s[76:77]
	global_load_dwordx2 v[218:219], v[186:187], off
	v_lshl_add_u64 v[186:187], v[186:187], 0, s[76:77]
	global_load_dwordx2 v[220:221], v[186:187], off
	v_lshl_add_u64 v[186:187], v[186:187], 0, s[76:77]
	global_load_dwordx2 v[222:223], v[186:187], off
	v_lshl_add_u64 v[186:187], v[186:187], 0, s[76:77]
	global_load_dwordx2 v[224:225], v[186:187], off
	v_lshl_add_u64 v[186:187], v[186:187], 0, s[76:77]
	global_load_dwordx2 v[226:227], v[186:187], off
	v_lshl_add_u64 v[186:187], v[186:187], 0, s[76:77]
	global_load_dwordx2 v[228:229], v[186:187], off
	v_lshl_add_u64 v[186:187], v[186:187], 0, s[76:77]
	global_load_dwordx2 v[230:231], v[186:187], off
	v_lshl_add_u64 v[186:187], v[186:187], 0, s[76:77]
	global_load_dwordx2 v[232:233], v[186:187], off
	v_lshl_add_u64 v[186:187], v[186:187], 0, s[76:77]
	global_load_dwordx2 v[234:235], v[186:187], off
	v_lshl_add_u64 v[186:187], v[186:187], 0, s[76:77]
	global_load_dwordx2 v[236:237], v[186:187], off
	v_lshl_add_u64 v[186:187], v[186:187], 0, s[76:77]
	global_load_dwordx2 v[238:239], v[186:187], off
	s_waitcnt vmcnt(16)
	s_branch .Lp8n_join
.Lp8n_skip:
	s_waitcnt vmcnt(0)
.Lp8n_join:
	v_or_b32_e32 v168, v182, v183
	v_cmp_ne_u32_e32 vcc, 0, v168
	s_and_saveexec_b64 s[34:35], vcc
	s_mov_b32 s64, s66
	s_cbranch_execz .LBB0_953
	v_cmp_ne_u32_sdwa s[38:39], v182, v169 src0_sel:BYTE_0 src1_sel:DWORD
	s_and_saveexec_b64 s[36:37], s[38:39]
	s_cbranch_execnz .LBB0_1106
	s_or_b64 exec, exec, s[36:37]
	v_cmp_ne_u32_sdwa s[38:39], v182, v169 src0_sel:BYTE_1 src1_sel:DWORD
	s_and_saveexec_b64 s[36:37], s[38:39]
	s_cbranch_execnz .LBB0_1107

.LBB0_1103:
	s_or_b64 exec, exec, s[34:35]
	s_waitcnt vmcnt(0)
	s_cmp_lg_u64 s[4:5], 0
	s_cbranch_scc0 .Lp8m_skip
	s_mov_b32 s75, 0
	v_cmp_ne_u32_e64 s[76:77], 0, v208
	s_cmp_lg_u64 s[76:77], 0
	s_cselect_b32 s78, 0x1, 0
	s_or_b32 s75, s75, s78
	v_cmp_ne_u32_e64 s[76:77], 0, v209
	s_cmp_lg_u64 s[76:77], 0
	s_cselect_b32 s78, 0x2, 0
	s_or_b32 s75, s75, s78
	v_cmp_ne_u32_e64 s[76:77], 0, v210
	s_cmp_lg_u64 s[76:77], 0
	s_cselect_b32 s78, 0x4, 0
	s_or_b32 s75, s75, s78
	v_cmp_ne_u32_e64 s[76:77], 0, v211
	s_cmp_lg_u64 s[76:77], 0
	s_cselect_b32 s78, 0x8, 0
	s_or_b32 s75, s75, s78
	v_cmp_ne_u32_e64 s[76:77], 0, v212
	s_cmp_lg_u64 s[76:77], 0
	s_cselect_b32 s78, 0x10, 0
	s_or_b32 s75, s75, s78
	v_cmp_ne_u32_e64 s[76:77], 0, v213
	s_cmp_lg_u64 s[76:77], 0
	s_cselect_b32 s78, 0x20, 0
	s_or_b32 s75, s75, s78
	v_cmp_ne_u32_e64 s[76:77], 0, v214
	s_cmp_lg_u64 s[76:77], 0
	s_cselect_b32 s78, 0x40, 0
	s_or_b32 s75, s75, s78
	v_cmp_ne_u32_e64 s[76:77], 0, v215
	s_cmp_lg_u64 s[76:77], 0
	s_cselect_b32 s78, 0x80, 0
	s_or_b32 s75, s75, s78
	v_cmp_ne_u32_e64 s[76:77], 0, v216
	s_cmp_lg_u64 s[76:77], 0
	s_cselect_b32 s78, 0x100, 0
	s_or_b32 s75, s75, s78
	v_cmp_ne_u32_e64 s[76:77], 0, v217
	s_cmp_lg_u64 s[76:77], 0
	s_cselect_b32 s78, 0x200, 0
	s_or_b32 s75, s75, s78
	v_cmp_ne_u32_e64 s[76:77], 0, v218
	s_cmp_lg_u64 s[76:77], 0
	s_cselect_b32 s78, 0x400, 0
	s_or_b32 s75, s75, s78
	v_cmp_ne_u32_e64 s[76:77], 0, v219
	s_cmp_lg_u64 s[76:77], 0
	s_cselect_b32 s78, 0x800, 0
	s_or_b32 s75, s75, s78
	v_cmp_ne_u32_e64 s[76:77], 0, v220
	s_cmp_lg_u64 s[76:77], 0
	s_cselect_b32 s78, 0x1000, 0
	s_or_b32 s75, s75, s78
	v_cmp_ne_u32_e64 s[76:77], 0, v221
	s_cmp_lg_u64 s[76:77], 0
	s_cselect_b32 s78, 0x2000, 0
	s_or_b32 s75, s75, s78
	v_cmp_ne_u32_e64 s[76:77], 0, v222
	s_cmp_lg_u64 s[76:77], 0
	s_cselect_b32 s78, 0x4000, 0
	s_or_b32 s75, s75, s78
	v_cmp_ne_u32_e64 s[76:77], 0, v223
	s_cmp_lg_u64 s[76:77], 0
	s_cselect_b32 s78, 0x8000, 0
	s_or_b32 s75, s75, s78
	v_cmp_ne_u32_e64 s[76:77], 0, v224
	s_cmp_lg_u64 s[76:77], 0
	s_cselect_b32 s78, 0x10000, 0
	s_or_b32 s75, s75, s78
	v_cmp_ne_u32_e64 s[76:77], 0, v225
	s_cmp_lg_u64 s[76:77], 0
	s_cselect_b32 s78, 0x20000, 0
	s_or_b32 s75, s75, s78
	v_cmp_ne_u32_e64 s[76:77], 0, v226
	s_cmp_lg_u64 s[76:77], 0
	s_cselect_b32 s78, 0x40000, 0
	s_or_b32 s75, s75, s78
	v_cmp_ne_u32_e64 s[76:77], 0, v227
	s_cmp_lg_u64 s[76:77], 0
	s_cselect_b32 s78, 0x80000, 0
	s_or_b32 s75, s75, s78
	v_cmp_ne_u32_e64 s[76:77], 0, v228
	s_cmp_lg_u64 s[76:77], 0
	s_cselect_b32 s78, 0x100000, 0
	s_or_b32 s75, s75, s78
	v_cmp_ne_u32_e64 s[76:77], 0, v229
	s_cmp_lg_u64 s[76:77], 0
	s_cselect_b32 s78, 0x200000, 0
	s_or_b32 s75, s75, s78
	v_cmp_ne_u32_e64 s[76:77], 0, v230
	s_cmp_lg_u64 s[76:77], 0
	s_cselect_b32 s78, 0x400000, 0
	s_or_b32 s75, s75, s78
	v_cmp_ne_u32_e64 s[76:77], 0, v231
	s_cmp_lg_u64 s[76:77], 0
	s_cselect_b32 s78, 0x800000, 0
	s_or_b32 s75, s75, s78
	v_cmp_ne_u32_e64 s[76:77], 0, v232
	s_cmp_lg_u64 s[76:77], 0
	s_cselect_b32 s78, 0x1000000, 0
	s_or_b32 s75, s75, s78
	v_cmp_ne_u32_e64 s[76:77], 0, v233
	s_cmp_lg_u64 s[76:77], 0
	s_cselect_b32 s78, 0x2000000, 0
	s_or_b32 s75, s75, s78
	v_cmp_ne_u32_e64 s[76:77], 0, v234
	s_cmp_lg_u64 s[76:77], 0
	s_cselect_b32 s78, 0x4000000, 0
	s_or_b32 s75, s75, s78
	v_cmp_ne_u32_e64 s[76:77], 0, v235
	s_cmp_lg_u64 s[76:77], 0
	s_cselect_b32 s78, 0x8000000, 0
	s_or_b32 s75, s75, s78
	v_cmp_ne_u32_e64 s[76:77], 0, v236
	s_cmp_lg_u64 s[76:77], 0
	s_cselect_b32 s78, 0x10000000, 0
	s_or_b32 s75, s75, s78
	v_cmp_ne_u32_e64 s[76:77], 0, v237
	s_cmp_lg_u64 s[76:77], 0
	s_cselect_b32 s78, 0x20000000, 0
	s_or_b32 s75, s75, s78
	v_cmp_ne_u32_e64 s[76:77], 0, v238
	s_cmp_lg_u64 s[76:77], 0
	s_cselect_b32 s78, 0x40000000, 0
	s_or_b32 s75, s75, s78
	v_cmp_ne_u32_e64 s[76:77], 0, v239
	s_cmp_lg_u64 s[76:77], 0
	s_cselect_b32 s78, 0x80000000, 0
	s_or_b32 s75, s75, s78
.Lp8m_skip:
	s_mov_b32 s74, s75
	s_andn2_b64 vcc, exec, s[4:5]
	s_mov_b64 s[4:5], -1
	s_cbranch_vccnz .LBB0_932
	s_andn2_b64 vcc, exec, s[8:9]
	s_cbranch_vccnz .LBB0_931
	s_barrier
	s_branch .LBB0_931
